# gather phase set-up: kernarg pointers, first token entries, gates and norm parameters requested up front (one memory round trip instead of five)
# baseline (speedup 1.0000x reference)
.LBB0_1401:
	s_andn2_b64 vcc, exec, s[0:1]
	s_cbranch_vccnz .LBB0_1479
	s_mov_b64 s[36:37], s[30:31]
	s_waitcnt vmcnt(0)
	v_mbcnt_lo_u32_b32 v0, -1, 0
	v_mbcnt_hi_u32_b32 v0, -1, v0
	s_nop 0
	v_add_u32_e32 v0, s3, v0
	s_nop 0
	v_readfirstlane_b32 s0, v0
	s_ashr_i32 s0, s0, 6
	s_add_i32 s44, s0, s67
	s_cmpk_gt_i32 s44, 0x3fff
	s_cbranch_scc1 .LBB0_1427
	s_load_dwordx2 s[4:5], s[36:37], 0xd8
	s_mul_i32 s74, s11, 0x3000
	v_and_b32_e32 v80, 63, v0
	v_lshrrev_b32_e32 v0, 2, v0
	v_lshlrev_b32_e32 v96, 6, v80
	s_waitcnt lgkmcnt(0)
	s_add_u32 s46, s4, 0x372ac000
	s_addc_u32 s47, s5, 0
	s_add_u32 s48, s4, 0x37aac000
	s_addc_u32 s49, s5, 0
	s_lshl_b64 s[50:51], s[74:75], 2
	s_add_u32 s8, s4, s50
	s_addc_u32 s9, s5, s51
	s_add_u32 s6, s4, 0xbaac000
	s_addc_u32 s88, s5, 0
	s_add_u32 s89, s4, 0xeaac000
	s_addc_u32 s92, s5, 0
	s_add_u32 s93, s4, 0xaaac000
	s_addc_u32 s20, s5, 0
	s_lshl_b32 s0, s0, 11
	s_add_i32 s21, s0, 0
	s_cmp_lg_u32 s11, 3
	s_cselect_b64 s[52:53], -1, 0
	s_add_u32 s84, s4, 0x4000
	s_addc_u32 s82, s5, 0
	v_and_b32_e32 v83, 12, v0
	v_lshl_add_u64 v[0:1], s[4:5], 0, v[96:97]
	s_cmp_eq_u32 s11, 1
	s_mov_b64 s[0:1], 0x1eaac000
	s_mov_b64 s[14:15], 0x1aaac000
	s_cselect_b64 s[54:55], -1, 0
	s_cmp_lg_u32 s11, 1
	v_lshl_add_u64 v[86:87], v[0:1], 0, s[0:1]
	s_mov_b64 s[0:1], 0x12aac000
	v_lshlrev_b32_e32 v96, 7, v80
	v_lshlrev_b32_e32 v82, 5, v80
	v_lshl_add_u64 v[84:85], v[0:1], 0, s[14:15]
	s_cselect_b64 s[34:35], -1, 0
	s_lshl_b32 s74, s11, 11
	v_lshl_add_u64 v[94:95], v[0:1], 0, s[0:1]
	v_lshl_add_u64 v[0:1], s[8:9], 0, v[96:97]
	s_mov_b64 s[0:1], 0xe000
	v_lshlrev_b32_e32 v81, 4, v80
	v_or_b32_e32 v89, 64, v80
	v_lshl_add_u32 v91, v80, 3, s21
	v_or_b32_e32 v88, 8, v82
	v_or_b32_e32 v90, 16, v82
	v_or_b32_e32 v92, 24, v82
	v_lshl_add_u64 v[98:99], v[0:1], 0, s[0:1]
	s_add_i32 s83, s21, 0x420
	s_lshl_b64 s[28:29], s[74:75], 2
	s_load_dwordx2 s[14:15], s[36:37], 0x28
	s_load_dwordx2 s[40:41], s[36:37], 0x68
	s_load_dwordx2 s[42:43], s[36:37], 0xc8
	s_load_dword s38, s[62:63], 0x0
	v_add_u32_e32 v0, s3, v80
	v_lshlrev_b32_e32 v1, 4, v0
	v_and_b32_e32 v2, 7, v0
	v_lshrrev_b32_e32 v3, 3, v0
	v_lshlrev_b32_e32 v2, 10, v2
	v_lshl_add_u32 v2, v3, 4, v2
	v_add_u32_e32 v2, 0x4000, v2
	v_add_u32_e32 v3, 0x4000, v2
	s_lshl_b32 s0, s44, 9
	v_lshl_add_u32 v26, v80, 2, s0
	global_load_dword v134, v26, s[46:47]
	global_load_dword v135, v26, s[46:47] offset:256
	global_load_dword v136, v26, s[48:49]
	global_load_dword v137, v26, s[48:49] offset:256
	s_add_u32 s0, s4, 0x4000
	s_addc_u32 s1, s5, 0
	s_add_u32 s8, s0, 0x34000
	s_addc_u32 s9, s1, 0
	s_mul_i32 s2, s11, 0xc000
	s_add_u32 s28, s0, s2
	s_addc_u32 s29, s1, 0
	s_add_u32 s28, s28, 0xa000
	s_addc_u32 s29, s29, 0
	global_load_dwordx4 v[4:7], v1, s[28:29]
	s_add_u32 s28, s8, s2
	s_addc_u32 s29, s9, 0
	s_add_u32 s28, s28, 0xa000
	s_addc_u32 s29, s29, 0
	global_load_dwordx4 v[8:11], v1, s[28:29]
	s_waitcnt lgkmcnt(0)
	s_lshl_b32 s38, s38, 3
	s_cmp_eq_u32 s11, 3
	s_cbranch_scc1 .Lgs_final
	s_cmp_eq_u32 s11, 1
	s_cbranch_scc1 .Lgs_l1
	s_add_i32 s10, s11, 1
	s_lshl_b32 s28, s10, 13
	s_mul_i32 s10, s10, 0xc000
	s_add_u32 s14, s14, s28
	s_addc_u32 s15, s15, 0
	global_load_dwordx4 v[12:15], v1, s[14:15]
	s_add_u32 s28, s0, s10
	s_addc_u32 s29, s1, 0
	global_load_dwordx4 v[16:19], v1, s[28:29]
	s_add_u32 s28, s28, 0x2000
	s_addc_u32 s29, s29, 0
	global_load_dwordx4 v[20:23], v1, s[28:29]
	s_add_u32 s28, s8, s10
	s_addc_u32 s29, s9, 0
	global_load_dwordx4 v[24:27], v1, s[28:29]
	s_add_u32 s28, s28, 0x2000
	s_addc_u32 s29, s29, 0
	global_load_dwordx4 v[28:31], v1, s[28:29]
	s_waitcnt vmcnt(0)
	ds_write_b128 v2, v[4:7]
	ds_write_b128 v2, v[8:11] offset:8192
	v_add_f32_e32 v20, 1.0, v20
	v_add_f32_e32 v21, 1.0, v21
	v_add_f32_e32 v22, 1.0, v22
	v_add_f32_e32 v23, 1.0, v23
	v_mul_f32_e32 v20, v12, v20
	v_mul_f32_e32 v21, v13, v21
	v_mul_f32_e32 v22, v14, v22
	v_mul_f32_e32 v23, v15, v23
	ds_write_b128 v2, v[20:23] offset:16384
	ds_write_b128 v2, v[16:19] offset:24576
	v_add_f32_e32 v28, 1.0, v28
	v_add_f32_e32 v29, 1.0, v29
	v_add_f32_e32 v30, 1.0, v30
	v_add_f32_e32 v31, 1.0, v31
	v_mul_f32_e32 v28, v12, v28
	v_mul_f32_e32 v29, v13, v29
	v_mul_f32_e32 v30, v14, v30
	v_mul_f32_e32 v31, v15, v31
	ds_write_b128 v3, v[28:31] offset:16384
	ds_write_b128 v3, v[24:27] offset:24576
	s_branch .Lgs_done
.Lgs_l1:
	s_mov_b32 s10, 0x30000
	global_load_dwordx4 v[12:15], v1, s[40:41]
	s_add_u32 s28, s0, s10
	s_addc_u32 s29, s1, 0
	global_load_dwordx4 v[16:19], v1, s[28:29]
	s_add_u32 s28, s28, 0x2000
	s_addc_u32 s29, s29, 0
	global_load_dwordx4 v[20:23], v1, s[28:29]
	s_add_u32 s28, s8, s10
	s_addc_u32 s29, s9, 0
	global_load_dwordx4 v[24:27], v1, s[28:29]
	s_add_u32 s28, s28, 0x2000
	s_addc_u32 s29, s29, 0
	global_load_dwordx4 v[28:31], v1, s[28:29]
	s_add_u32 s14, s14, 0x4000
	s_addc_u32 s15, s15, 0
	global_load_dwordx4 v[32:35], v1, s[14:15]
	s_add_u32 s28, s0, 0x18000
	s_addc_u32 s29, s1, 0
	global_load_dwordx4 v[36:39], v1, s[28:29]
	s_add_u32 s28, s28, 0x2000
	s_addc_u32 s29, s29, 0
	global_load_dwordx4 v[40:43], v1, s[28:29]
	s_add_u32 s28, s8, 0x18000
	s_addc_u32 s29, s9, 0
	global_load_dwordx4 v[44:47], v1, s[28:29]
	s_add_u32 s28, s28, 0x2000
	s_addc_u32 s29, s29, 0
	global_load_dwordx4 v[48:51], v1, s[28:29]
	s_waitcnt vmcnt(0)
	ds_write_b128 v2, v[4:7]
	ds_write_b128 v2, v[8:11] offset:8192
	v_add_f32_e32 v20, 1.0, v20
	v_add_f32_e32 v21, 1.0, v21
	v_add_f32_e32 v22, 1.0, v22
	v_add_f32_e32 v23, 1.0, v23
	v_mul_f32_e32 v20, v12, v20
	v_mul_f32_e32 v21, v13, v21
	v_mul_f32_e32 v22, v14, v22
	v_mul_f32_e32 v23, v15, v23
	ds_write_b128 v2, v[20:23] offset:16384
	ds_write_b128 v2, v[16:19] offset:24576
	v_add_f32_e32 v28, 1.0, v28
	v_add_f32_e32 v29, 1.0, v29
	v_add_f32_e32 v30, 1.0, v30
	v_add_f32_e32 v31, 1.0, v31
	v_mul_f32_e32 v28, v12, v28
	v_mul_f32_e32 v29, v13, v29
	v_mul_f32_e32 v30, v14, v30
	v_mul_f32_e32 v31, v15, v31
	ds_write_b128 v3, v[28:31] offset:16384
	ds_write_b128 v3, v[24:27] offset:24576
	v_add_f32_e32 v40, 1.0, v40
	v_add_f32_e32 v41, 1.0, v41
	v_add_f32_e32 v42, 1.0, v42
	v_add_f32_e32 v43, 1.0, v43
	v_mul_f32_e32 v40, v32, v40
	v_mul_f32_e32 v41, v33, v41
	v_mul_f32_e32 v42, v34, v42
	v_mul_f32_e32 v43, v35, v43
	ds_write_b128 v2, v[40:43] offset:49152
	ds_write_b128 v2, v[36:39] offset:57344
	v_add_f32_e32 v48, 1.0, v48
	v_add_f32_e32 v49, 1.0, v49
	v_add_f32_e32 v50, 1.0, v50
	v_add_f32_e32 v51, 1.0, v51
	v_mul_f32_e32 v48, v32, v48
	v_mul_f32_e32 v49, v33, v49
	v_mul_f32_e32 v50, v34, v50
	v_mul_f32_e32 v51, v35, v51
	ds_write_b128 v3, v[48:51] offset:49152
	ds_write_b128 v3, v[44:47] offset:57344
	s_branch .Lgs_done
.Lgs_final:
	global_load_dwordx4 v[12:15], v1, s[42:43]
	s_waitcnt vmcnt(0)
	ds_write_b128 v2, v[4:7]
	ds_write_b128 v2, v[8:11] offset:8192
	ds_write_b128 v2, v[12:15] offset:16384
